# MoBA attention loop: next tile's 4 LDS-DMA pieces issued one per MFMA gap behind the first QK MFMAs (as in the MLA loop)
# speedup vs baseline: 1.0267x; 1.0006x over previous
; template <bool MLA>
; __device__ __forceinline__ void attn_unit(char* lds, int h, int qb, const bf16_t* Qp, int ldq, const bf16_t* Kp, int ldk, const bf16_t* KRp, const bf16_t* Vp, int ldv,
;                                           unsigned char* Op, int ldo, const float* KMp, const float* rel_bias) {
;     ...
;             { const int vb0 = vrb + buf * SHM_V;
;     ...
;               PV_D0(0); PV_D0(1); PV_D0(2); PV_D0(3);
.LBB0_1553:
	v_add_f32_e32 v100, v84, v85
	v_fmac_f32_e32 v100, v216, v2
	v_add_u32_e32 v2, s75, v194
	ds_read_b64_tr_b16 v[84:85], v2 offset:0
	ds_read_b64_tr_b16 v[86:87], v2 offset:0x800
	ds_read_b64_tr_b16 v[88:89], v2 offset:0x1000
	ds_read_b64_tr_b16 v[90:91], v2 offset:0x1800
	ds_read_b64_tr_b16 v[92:93], v2 offset:0x2000
	ds_read_b64_tr_b16 v[94:95], v2 offset:0x2800
	ds_read_b64_tr_b16 v[96:97], v2 offset:0x3000
	ds_read_b64_tr_b16 v[98:99], v2 offset:0x3800
	s_waitcnt lgkmcnt(0)
	s_nop 0
	v_mfma_f32_32x32x16_bf16 v[52:67], v[68:71], v[84:87], v[52:67]
	v_mfma_f32_32x32x16_bf16 v[52:67], v[72:75], v[88:91], v[52:67]
	v_mfma_f32_32x32x16_bf16 v[52:67], v[76:79], v[92:95], v[52:67]
	v_mfma_f32_32x32x16_bf16 v[52:67], v[80:83], v[96:99], v[52:67]
	ds_read_b64_tr_b16 v[84:85], v2 offset:0x200
	ds_read_b64_tr_b16 v[86:87], v2 offset:0xa00
	ds_read_b64_tr_b16 v[88:89], v2 offset:0x1200
	ds_read_b64_tr_b16 v[90:91], v2 offset:0x1a00
	ds_read_b64_tr_b16 v[92:93], v2 offset:0x2200
	ds_read_b64_tr_b16 v[94:95], v2 offset:0x2a00
	ds_read_b64_tr_b16 v[96:97], v2 offset:0x3200
	ds_read_b64_tr_b16 v[98:99], v2 offset:0x3a00
	s_waitcnt lgkmcnt(0)
	s_nop 0
	v_mfma_f32_32x32x16_bf16 v[36:51], v[68:71], v[84:87], v[36:51]
	v_mfma_f32_32x32x16_bf16 v[36:51], v[72:75], v[88:91], v[36:51]
	v_mfma_f32_32x32x16_bf16 v[36:51], v[76:79], v[92:95], v[36:51]
	v_mfma_f32_32x32x16_bf16 v[36:51], v[80:83], v[96:99], v[36:51]
	ds_read_b64_tr_b16 v[84:85], v2 offset:0x400
	ds_read_b64_tr_b16 v[86:87], v2 offset:0xc00
	ds_read_b64_tr_b16 v[88:89], v2 offset:0x1400
	ds_read_b64_tr_b16 v[90:91], v2 offset:0x1c00
	ds_read_b64_tr_b16 v[92:93], v2 offset:0x2400
	ds_read_b64_tr_b16 v[94:95], v2 offset:0x2c00
	ds_read_b64_tr_b16 v[96:97], v2 offset:0x3400
	ds_read_b64_tr_b16 v[98:99], v2 offset:0x3c00
	s_waitcnt lgkmcnt(0)
	s_nop 0
	v_mfma_f32_32x32x16_bf16 v[20:35], v[68:71], v[84:87], v[20:35]
	v_mfma_f32_32x32x16_bf16 v[20:35], v[72:75], v[88:91], v[20:35]
	v_mfma_f32_32x32x16_bf16 v[20:35], v[76:79], v[92:95], v[20:35]
	v_mfma_f32_32x32x16_bf16 v[20:35], v[80:83], v[96:99], v[20:35]
	ds_read_b64_tr_b16 v[84:85], v2 offset:0x600
	ds_read_b64_tr_b16 v[86:87], v2 offset:0xe00
	ds_read_b64_tr_b16 v[88:89], v2 offset:0x1600
	ds_read_b64_tr_b16 v[90:91], v2 offset:0x1e00
	ds_read_b64_tr_b16 v[92:93], v2 offset:0x2600
	ds_read_b64_tr_b16 v[94:95], v2 offset:0x2e00
	ds_read_b64_tr_b16 v[96:97], v2 offset:0x3600
	ds_read_b64_tr_b16 v[98:99], v2 offset:0x3e00
	s_waitcnt lgkmcnt(0)
	s_nop 0
	v_mfma_f32_32x32x16_bf16 v[4:19], v[68:71], v[84:87], v[4:19]
	v_mfma_f32_32x32x16_bf16 v[4:19], v[72:75], v[88:91], v[4:19]
	v_mfma_f32_32x32x16_bf16 v[4:19], v[76:79], v[92:95], v[4:19]
	v_mfma_f32_32x32x16_bf16 v[4:19], v[80:83], v[96:99], v[4:19]
	v_mov_b32_e32 v216, v100
	s_branch .LBB0_1554
.Lmoba_inact:
	s_xor_b32 s100, s75, 0x4000
	s_add_i32 s100, s27, s100
	v_lshl_add_u64 v[228:229], s[52:53], 0, v[182:183]
	s_add_i32 m0, s100, 0x8000
	s_nop 0
	global_load_lds_dwordx4 v[228:229], off
	v_lshl_add_u64 v[228:229], s[52:53], 0, v[180:181]
	v_lshl_add_u64 v[230:231], v[228:229], 0, s[46:47]
	s_mov_b32 m0, s100
	v_lshl_add_u64 v[228:229], v[228:229], 0, s[48:49]
	global_load_lds_dwordx4 v[230:231], off
	v_lshl_add_u64 v[230:231], s[52:53], 0, v[184:185]
	s_add_i32 m0, s100, 0x8400
	s_nop 0
	global_load_lds_dwordx4 v[230:231], off
	s_add_i32 m0, s100, 0x400
	s_nop 0
	global_load_lds_dwordx4 v[228:229], off

; template <bool MLA>
; __device__ __forceinline__ void attn_unit(char* lds, int h, int qb, const bf16_t* Qp, int ldq, const bf16_t* Kp, int ldk, const bf16_t* KRp, const bf16_t* Vp, int ldv,
;                                           unsigned char* Op, int ldo, const float* KMp, const float* rel_bias) {
;     ...
;         const int buf = t & 1, kb = t * 64, jb = kb >> 8;
;         if (t + 1 < NT) A_ISSUE(kb + 64, buf ^ 1);
;         int act;
;         if (MLA || jb == qb) act = (kb <= qlo + 31) ? 1 : 0; else act = __any((int)((mysel >> jb) & 1u)) ? 1 : 0;
;         act = __builtin_amdgcn_readfirstlane(act);
.LBB0_1555:
	s_and_b32 s75, s72, 0x4000
	s_lshr_b32 s76, s68, 8
	s_mov_b64 s[56:57], -1
	s_cmp_eq_u32 s76, s26
	s_cselect_b64 s[12:13], -1, 0
	s_cmp_lg_u32 s76, s26
	s_cbranch_scc0 .LBB0_1557
	v_bfe_u32 v2, v219, s76, 1
	v_cmp_ne_u32_e32 vcc, 0, v2
	s_cmp_lg_u64 vcc, 0
	s_mov_b64 s[56:57], 0
	s_cselect_b64 s[54:55], -1, 0

; template <bool MLA>
; __device__ __forceinline__ void attn_unit(char* lds, int h, int qb, const bf16_t* Qp, int ldq, const bf16_t* Kp, int ldk, const bf16_t* KRp, const bf16_t* Vp, int ldv,
;                                           unsigned char* Op, int ldo, const float* KMp, const float* rel_bias) {
;     ...
;         if (MLA || jb == qb) act = (kb <= qlo + 31) ? 1 : 0; else act = __any((int)((mysel >> jb) & 1u)) ? 1 : 0;
;         act = __builtin_amdgcn_readfirstlane(act);
;         if (act) {
;             f32x16 p0, p1;
; #pragma unroll
;             for (int r = 0; r < 16; ++r) { p0[r] = 0.f; p1[r] = 0.f; }
;             { const char* kn = lds + buf * SHM_KN; const char* kr = lds + buf * SHM_KR;
; #pragma unroll
;               for (int d0 = 0; d0 < 8; ++d0) { const char* ap = kn + kan[d0 & 3] + (d0 >> 2) * 128;
;                   const bf16x8 a0 = *(const bf16x8*)ap, a1 = *(const bf16x8*)(ap + 32 * 256);
;                   p0 = __builtin_amdgcn_mfma_f32_32x32x16_bf16(a0, qr[d0], p0, 0, 0, 0);
;                   p1 = __builtin_amdgcn_mfma_f32_32x32x16_bf16(a1, qr[d0], p1, 0, 0, 0); }
;               if constexpr (MLA) {
; #pragma unroll
;                   for (int d0 = 8; d0 < 12; ++d0) { const char* ap = kr + kar[d0 & 3];
;                       const bf16x8 a0 = *(const bf16x8*)ap, a1 = *(const bf16x8*)(ap + 32 * 128);
;                       p0 = __builtin_amdgcn_mfma_f32_32x32x16_bf16(a0, qr[d0], p0, 0, 0, 0);
;                       p1 = __builtin_amdgcn_mfma_f32_32x32x16_bf16(a1, qr[d0], p1, 0, 0, 0); } } }
;             const int dq = qpos - kb - 4 * hi;
;             if constexpr (MLA) {
;                 if (kb + 63 > qlo) {
; #pragma unroll
;                     for (int r = 0; r < 16; ++r) { const int d0 = dq - CROWC(r); if (d0 < 0) p0[r] = NEG; if (d0 < 32) p1[r] = NEG; } }
;             } else {
;                 const bool selq = (jb == qb) || (((mysel >> jb) & 1u) != 0u);
;                 if (q0 - (kb + 63) >= 128) { const float cb = bt_l[128];
; #pragma unroll
;                     for (int r = 0; r < 16; ++r) { p0[r] = selq ? p0[r] + cb : NEG; p1[r] = selq ? p1[r] + cb : NEG; } }
;                 else {
; #pragma unroll
;                     for (int r4 = 0; r4 < 4; ++r4) {
; #pragma unroll
;                         for (int rr = 0; rr < 4; ++rr) { const int r = r4 * 4 + rr; const int d0 = dq - CROWC(r), d1 = d0 - 32;
.LBB0_1559:
	v_cndmask_b32_e64 v2, 0, 1, s[54:55]
	s_nop 0
	v_readfirstlane_b32 s22, v2
	s_bitcmp0_b32 s22, 0
	s_cbranch_scc1 .Lmoba_inact
	s_add_i32 s22, s75, 0
	v_add_u32_e32 v2, s22, v203
	ds_read_b128 v[68:71], v2 offset:32768
	ds_read_b128 v[72:75], v2 offset:32896
	s_mov_b64 s[54:55], -1
	s_waitcnt lgkmcnt(0)
	v_mfma_f32_32x32x16_bf16 v[100:115], v[68:71], v[160:163], 0
	s_xor_b32 s100, s75, 0x4000
	s_add_i32 s100, s27, s100
	v_lshl_add_u64 v[228:229], s[52:53], 0, v[182:183]
	s_add_i32 m0, s100, 0x8000
	s_nop 0
	global_load_lds_dwordx4 v[228:229], off
	ds_read_b128 v[68:71], v2 offset:40960
	ds_read_b128 v[76:79], v2 offset:41088
	v_add_u32_e32 v2, s22, v204
	s_waitcnt lgkmcnt(0)
	v_mfma_f32_32x32x16_bf16 v[84:99], v[68:71], v[160:163], 0
	v_lshl_add_u64 v[228:229], s[52:53], 0, v[180:181]
	v_lshl_add_u64 v[230:231], v[228:229], 0, s[46:47]
	s_mov_b32 m0, s100
	v_lshl_add_u64 v[228:229], v[228:229], 0, s[48:49]
	global_load_lds_dwordx4 v[230:231], off
	ds_read_b128 v[68:71], v2 offset:32768
	ds_read_b128 v[80:83], v2 offset:32896
	s_waitcnt lgkmcnt(0)
	v_mfma_f32_32x32x16_bf16 v[100:115], v[68:71], v[156:159], v[100:115]
	v_lshl_add_u64 v[230:231], s[52:53], 0, v[184:185]
	s_add_i32 m0, s100, 0x8400
	s_nop 0
	global_load_lds_dwordx4 v[230:231], off
	ds_read_b128 v[68:71], v2 offset:40960
	ds_read_b128 v[116:119], v2 offset:41088
	v_add_u32_e32 v2, s22, v205
	s_waitcnt lgkmcnt(0)
	v_mfma_f32_32x32x16_bf16 v[84:99], v[68:71], v[156:159], v[84:99]
	s_add_i32 m0, s100, 0x400
	s_nop 0
	global_load_lds_dwordx4 v[228:229], off
	ds_read_b128 v[68:71], v2 offset:32768
	ds_read_b128 v[120:123], v2 offset:32896
	s_waitcnt lgkmcnt(0)
	v_mfma_f32_32x32x16_bf16 v[100:115], v[68:71], v[152:155], v[100:115]
	ds_read_b128 v[68:71], v2 offset:40960
	ds_read_b128 v[124:127], v2 offset:41088
	v_add_u32_e32 v2, s22, v206
	s_lshl_b32 s22, 1, s76
	s_waitcnt lgkmcnt(0)
	v_mfma_f32_32x32x16_bf16 v[84:99], v[68:71], v[152:155], v[84:99]
	ds_read_b128 v[68:71], v2 offset:32768
	ds_read_b128 v[128:131], v2 offset:32896
	s_waitcnt lgkmcnt(0)
	v_mfma_f32_32x32x16_bf16 v[100:115], v[68:71], v[148:151], v[100:115]
	ds_read_b128 v[68:71], v2 offset:40960
	ds_read_b128 v[222:225], v2 offset:41088
	v_and_b32_e32 v2, s22, v219
	v_cmp_ne_u32_e32 vcc, 0, v2
	s_or_b64 s[12:13], s[12:13], vcc
	s_cmpk_gt_i32 s69, 0x7f
	s_waitcnt lgkmcnt(0)
	v_mfma_f32_32x32x16_bf16 v[84:99], v[68:71], v[148:151], v[84:99]
	v_mfma_f32_32x32x16_bf16 v[100:115], v[72:75], v[144:147], v[100:115]
	v_mfma_f32_32x32x16_bf16 v[84:99], v[76:79], v[144:147], v[84:99]
	v_mfma_f32_32x32x16_bf16 v[100:115], v[80:83], v[140:143], v[100:115]
	v_mfma_f32_32x32x16_bf16 v[84:99], v[116:119], v[140:143], v[84:99]
	v_mfma_f32_32x32x16_bf16 v[100:115], v[120:123], v[136:139], v[100:115]
	v_mfma_f32_32x32x16_bf16 v[84:99], v[124:127], v[136:139], v[84:99]
	v_mfma_f32_32x32x16_bf16 v[100:115], v[128:131], v[132:135], v[100:115]
	v_mfma_f32_32x32x16_bf16 v[84:99], v[222:225], v[132:135], v[84:99]
	s_cbranch_scc1 .LBB0_1594
	v_add_u32_e32 v117, s69, v220
	v_add_u32_e32 v2, 63, v117
	v_med3_i32 v68, v2, 32, v214
	v_lshl_add_u32 v68, v68, 2, s16
	v_add_u32_e32 v68, 0xffffff80, v68
	ds_read_b32 v116, v68
	v_cmp_lt_i32_e32 vcc, -1, v2
	s_and_b64 s[56:57], vcc, s[12:13]
	v_mov_b32_e32 v69, 0xff800000
	v_mov_b32_e32 v68, 0xff800000
	s_and_saveexec_b64 s[54:55], s[56:57]
	s_cbranch_execz .LBB0_1563
	v_min_u32_e32 v68, 0x80, v2
	v_lshl_add_u32 v68, v68, 2, 0
	v_add_u32_e32 v68, 0x14c00, v68
	ds_read_b32 v68, v68
	s_waitcnt lgkmcnt(0)
	v_add_f32_e32 v68, v100, v68
